# baseline (speedup 1.0000x reference)
_Z10attn64_fwdPKtS0_S0_Pt8PrepArgs:
	s_mov_b64 s[4:5], -1
	s_cmpk_lt_u32 s2, 0x300
	v_lshlrev_b32_e32 v1, 4, v0
	s_cbranch_scc0 .LBB1_53
	s_bitcmp1_b32 s2, 8
	s_cbranch_scc0 .Lattn_noprio
	s_setprio 1
.Lattn_noprio:
	s_lshr_b32 s12, s2, 4
	s_and_b32 s3, s2, 7
	s_and_b32 s12, s12, 56
	s_or_b32 s3, s12, s3
	s_mul_i32 s12, s3, 43
	s_lshr_b32 s14, s12, 9
	s_mul_i32 s12, s14, 12
	v_readfirstlane_b32 s15, v0
	s_lshl_b32 s13, s2, 4
	s_load_dwordx8 s[4:11], s[0:1], 0x0
	s_sub_i32 s3, s3, s12
	s_lshr_b32 s24, s15, 6
	s_lshl_b32 s12, s14, 11
	s_and_b32 s13, s13, 0x780
	s_or_b32 s12, s12, s13
	s_lshl_b32 s13, s24, 5
	s_add_i32 s12, s12, s13
	s_mul_hi_u32 s13, s12, 0x300
	s_mulk_i32 s12, 0x300
	s_lshl_b64 s[12:13], s[12:13], 1
	s_waitcnt lgkmcnt(0)
	s_add_u32 s4, s4, s12
	s_addc_u32 s5, s5, s13
	s_and_b32 s16, s3, 0xff
	s_lshl_b32 s3, s16, 6
	s_lshl_b32 s17, s16, 7
	s_add_u32 s18, s4, s17
	s_addc_u32 s19, s5, 0
	s_and_b32 s16, s15, 0x3fffffc0
	s_mul_i32 s14, s14, 0x300000
	s_add_u32 s4, s6, s14
	v_and_b32_e32 v212, 63, v0
	s_addc_u32 s5, s7, 0
	s_add_u32 s4, s4, s17
	v_mul_u32_u24_e32 v2, 0x300, v212
	s_addc_u32 s5, s5, 0
	v_lshlrev_b32_e32 v200, 1, v2
	v_mov_b32_e32 v201, 0
	s_lshl_b32 s20, s24, 4
	v_lshl_add_u64 v[2:3], s[4:5], 0, v[200:201]
	s_add_u32 s4, s8, s14
	s_addc_u32 s5, s9, 0
	s_mov_b32 s21, 0
	s_add_u32 s4, s4, s17
	v_lshl_add_u64 v[198:199], v[2:3], 0, s[20:21]
	s_addc_u32 s5, s5, 0
	v_bfe_u32 v2, v0, 2, 4
	s_lshr_b32 s6, s15, 2
	v_and_or_b32 v2, s6, 48, v2
	v_mul_u32_u24_e32 v2, 0x300, v2
	s_and_b32 s20, s6, 0x3fffffc0
	s_lshl_b32 s27, s24, 10
	v_lshlrev_b32_e32 v200, 1, v2
	s_cmp_lg_u32 0, -1
	v_lshl_add_u64 v[2:3], s[4:5], 0, v[200:201]
	v_lshlrev_b32_e32 v213, 3, v0
	s_cselect_b32 s4, 0, 0
	v_and_b32_e32 v50, 24, v213
	s_add_i32 s29, s27, s4
	s_mov_b32 s4, m0
	s_mov_b32 m0, s29
	s_nop 0
	global_load_lds_dwordx4 v[198:199], off
	s_mov_b32 m0, s4
	v_lshl_add_u64 v[2:3], v[2:3], 0, s[20:21]
	v_lshlrev_b32_e32 v200, 1, v50
	v_lshl_add_u64 v[194:195], v[198:199], 0, 64
	s_add_i32 s28, s29, 0x1000
	s_mov_b32 s4, m0
	s_mov_b32 m0, s28
	s_nop 0
	global_load_lds_dwordx4 v[194:195], off
	s_mov_b32 m0, s4
	v_lshl_add_u64 v[202:203], v[2:3], 0, v[200:201]
	s_add_i32 s26, s29, 0x6000
	s_mov_b32 s4, m0
	s_mov_b32 m0, s26
	s_nop 0
	global_load_lds_dwordx4 v[202:203], off
	s_mov_b32 m0, s4
	v_lshl_add_u64 v[196:197], v[202:203], 0, 64
	s_add_i32 s25, s29, 0x7000
	s_mov_b32 s4, m0
	s_mov_b32 m0, s25
	s_nop 0
	global_load_lds_dwordx4 v[196:197], off
	s_mov_b32 m0, s4
	s_mov_b64 s[4:5], 0x18000
	v_lshl_add_u64 v[2:3], v[198:199], 0, s[4:5]
	s_mov_b64 s[14:15], 0x18040
	v_and_b32_e32 v214, 31, v0
	v_bfe_u32 v215, v0, 5, 1
	s_add_i32 s6, s29, 0x2000
	s_mov_b32 s7, m0
	s_mov_b32 m0, s6
	s_nop 0
	global_load_lds_dwordx4 v[2:3], off
	s_mov_b32 m0, s7
	v_lshl_add_u64 v[2:3], v[198:199], 0, s[14:15]
	s_add_i32 s6, s29, 0x3000
	s_mov_b32 s7, m0
	s_mov_b32 m0, s6
	s_nop 0
	global_load_lds_dwordx4 v[2:3], off
	s_mov_b32 m0, s7
	v_mul_u32_u24_e32 v2, 0x300, v214
	v_lshlrev_b32_e32 v200, 4, v215
	v_lshl_or_b32 v2, v2, 1, v200
	global_load_dwordx4 v[174:177], v2, s[18:19]
	global_load_dwordx4 v[170:173], v2, s[18:19] offset:32
	global_load_dwordx4 v[166:169], v2, s[18:19] offset:64
	global_load_dwordx4 v[162:165], v2, s[18:19] offset:96
	s_mov_b64 s[6:7], 0x30000
	s_mov_b64 s[8:9], 0x30040
	v_lshlrev_b32_e32 v2, 10, v215
	v_lshlrev_b32_e32 v3, 4, v214
	v_add3_u32 v218, 0, v2, v3
	v_lshl_add_u64 v[2:3], v[198:199], 0, s[6:7]
	v_lshl_add_u64 v[4:5], v[198:199], 0, s[8:9]
	s_add_i32 s8, s29, 0x4000
	s_mov_b32 s17, m0
	s_mov_b32 m0, s8
	s_nop 0
	global_load_lds_dwordx4 v[2:3], off
	s_mov_b32 m0, s17
	s_add_i32 s9, s29, 0x5000
	s_mov_b32 s8, m0
	s_mov_b32 m0, s9
	s_nop 0
	global_load_lds_dwordx4 v[4:5], off
	s_mov_b32 m0, s8
	s_waitcnt vmcnt(6) lgkmcnt(0)
	s_barrier
	ds_read_b128 v[2:5], v218
	ds_read_b128 v[6:9], v218 offset:512
	ds_read_b128 v[34:37], v218 offset:2048
	ds_read_b128 v[38:41], v218 offset:2560
	s_mov_b64 s[8:9], 0x48000
	s_mov_b64 s[18:19], 0x48040
	s_mov_b32 s31, -1
	s_movk_i32 s35, 0x2000
	s_movk_i32 s33, 0x4000
	s_mov_b32 s34, 0x41000000
	s_waitcnt vmcnt(3) lgkmcnt(3)
	v_mfma_f32_32x32x16_f16 v[18:33], v[2:5], v[174:177], 0
	s_waitcnt lgkmcnt(2)
	v_mfma_f32_32x32x16_f16 v[2:17], v[6:9], v[174:177], 0
	s_waitcnt vmcnt(2) lgkmcnt(1)
	v_mfma_f32_32x32x16_f16 v[18:33], v[34:37], v[170:173], v[18:33]
	s_waitcnt lgkmcnt(0)
	v_mfma_f32_32x32x16_f16 v[2:17], v[38:41], v[170:173], v[2:17]
	ds_read_b128 v[34:37], v218 offset:4096
	ds_read_b128 v[38:41], v218 offset:4608
	s_waitcnt vmcnt(1) lgkmcnt(1)
	v_mfma_f32_32x32x16_f16 v[18:33], v[34:37], v[166:169], v[18:33]
	s_waitcnt lgkmcnt(0)
	v_mfma_f32_32x32x16_f16 v[2:17], v[38:41], v[166:169], v[2:17]
	ds_read_b128 v[34:37], v218 offset:6144
	ds_read_b128 v[38:41], v218 offset:6656
	s_waitcnt vmcnt(0) lgkmcnt(1)
	v_mfma_f32_32x32x16_f16 v[18:33], v[34:37], v[162:165], v[18:33]
	s_waitcnt lgkmcnt(0)
	v_mfma_f32_32x32x16_f16 v[2:17], v[38:41], v[162:165], v[2:17]
	s_nop 9
	v_max_f32_e32 v34, v19, v19
	v_max_f32_e32 v35, v18, v18
	v_max_f32_e32 v34, v35, v34
	v_max3_f32 v36, v20, v21, v3
	v_max3_f32 v34, v34, v2, v4
	v_max3_f32 v35, v36, v24, v25
	v_max3_f32 v34, v34, v5, v22
	v_max3_f32 v35, v35, v8, v9
	v_max3_f32 v34, v34, v23, v6
	v_max3_f32 v35, v35, v28, v29
	v_max3_f32 v34, v34, v7, v26
	v_max3_f32 v35, v35, v12, v13
	v_max3_f32 v34, v34, v27, v10
	v_max3_f32 v35, v35, v32, v33
	v_max3_f32 v34, v34, v11, v30
	v_max3_f32 v35, v35, v16, v17
	v_max3_f32 v34, v34, v31, v14
	v_max3_f32 v34, v34, v15, v35
	v_mov_b32_e32 v35, v34
	s_nop 1
	v_permlane32_swap_b32_e32 v34, v35
	v_max_f32_e32 v35, v35, v35
	v_max_f32_e32 v34, v34, v34
	v_max_f32_e32 v219, v34, v35
	v_xor_b32_e32 v34, 0x80000000, v219
	v_mov_b32_e32 v35, v34
	v_mov_b32_e32 v36, v34
	v_mov_b32_e32 v37, v34
	v_mov_b32_e32 v38, v34
	v_mov_b32_e32 v39, v34
	v_mov_b32_e32 v40, v34
	v_mov_b32_e32 v41, v34
	v_mov_b32_e32 v42, v34
	v_mov_b32_e32 v43, v34
	v_mov_b32_e32 v44, v34
	v_mov_b32_e32 v45, v34
	v_mov_b32_e32 v46, v34
	v_mov_b32_e32 v47, v34
	v_mov_b32_e32 v48, v34
	v_mov_b32_e32 v49, v34
	s_waitcnt vmcnt(0) lgkmcnt(0)
	s_barrier
	v_sub_f32_e32 v51, v2, v219
	v_sub_f32_e32 v52, v3, v219
	v_lshl_add_u64 v[2:3], v[198:199], 0, s[8:9]
	s_mov_b32 s17, m0
	s_mov_b32 m0, s29
	s_nop 0
	global_load_lds_dwordx4 v[2:3], off
	s_mov_b32 m0, s17
	v_lshl_add_u64 v[2:3], v[198:199], 0, s[18:19]
	s_mov_b32 s17, m0
	s_mov_b32 m0, s28
	s_nop 0
	global_load_lds_dwordx4 v[2:3], off
	s_mov_b32 m0, s17
	s_add_i32 s17, s29, 0x8000
	v_lshl_add_u64 v[2:3], v[202:203], 0, s[4:5]
	s_mov_b32 s4, m0
	s_mov_b32 m0, s17
	s_nop 0
	global_load_lds_dwordx4 v[2:3], off
	s_mov_b32 m0, s4
	s_add_i32 s4, s29, 0x9000
	v_lshl_add_u64 v[2:3], v[202:203], 0, s[14:15]
	s_mov_b32 s5, m0
	s_mov_b32 m0, s4
	s_nop 0
	global_load_lds_dwordx4 v[2:3], off
	s_mov_b32 m0, s5
	ds_read_b128 v[82:85], v218 offset:8192
	ds_read_b128 v[182:185], v218 offset:8704
	ds_read_b128 v[178:181], v218 offset:10240
	ds_read_b128 v[142:145], v218 offset:10752
	ds_read_b128 v[138:141], v218 offset:12288
	ds_read_b128 v[134:137], v218 offset:12800
	ds_read_b128 v[130:133], v218 offset:14336
	ds_read_b128 v[126:129], v218 offset:14848
	v_lshlrev_b32_e32 v2, 1, v0
	v_and_b32_e32 v2, 32, v2
	v_sub_f32_e32 v18, v18, v219
	v_sub_f32_e32 v19, v19, v219
	v_sub_f32_e32 v20, v20, v219
	v_sub_f32_e32 v21, v21, v219
	v_sub_f32_e32 v22, v22, v219
	v_sub_f32_e32 v23, v23, v219
	v_sub_f32_e32 v24, v24, v219
	v_sub_f32_e32 v25, v25, v219
	v_sub_f32_e32 v26, v26, v219
	v_sub_f32_e32 v27, v27, v219
	v_sub_f32_e32 v28, v28, v219
	v_sub_f32_e32 v29, v29, v219
	v_sub_f32_e32 v30, v30, v219
	v_sub_f32_e32 v31, v31, v219
	v_sub_f32_e32 v32, v32, v219
	v_sub_f32_e32 v33, v33, v219
	v_sub_f32_e32 v4, v4, v219
	v_sub_f32_e32 v5, v5, v219
	v_sub_f32_e32 v6, v6, v219
	v_sub_f32_e32 v7, v7, v219
	v_sub_f32_e32 v8, v8, v219
	v_sub_f32_e32 v9, v9, v219
	v_sub_f32_e32 v10, v10, v219
	v_sub_f32_e32 v11, v11, v219
	v_sub_f32_e32 v12, v12, v219
	v_sub_f32_e32 v13, v13, v219
	v_sub_f32_e32 v14, v14, v219
	v_sub_f32_e32 v15, v15, v219
	v_sub_f32_e32 v16, v16, v219
	v_sub_f32_e32 v17, v17, v219
	v_add3_u32 v2, 0, v2, v50
	v_lshlrev_b32_e32 v3, 8, v215
	v_and_b32_e32 v50, 0xc0, v1
	v_add3_u32 v216, v2, v3, v50
	v_exp_f32_e32 v66, v18
	v_exp_f32_e32 v67, v19
	v_exp_f32_e32 v50, v51
	v_exp_f32_e32 v51, v52
	v_exp_f32_e32 v68, v20
	v_exp_f32_e32 v52, v4
	v_exp_f32_e32 v69, v21
	v_exp_f32_e32 v53, v5
	v_exp_f32_e32 v70, v22
	v_exp_f32_e32 v54, v6
	v_exp_f32_e32 v71, v23
	v_exp_f32_e32 v55, v7
	v_exp_f32_e32 v72, v24
	v_exp_f32_e32 v56, v8
	v_exp_f32_e32 v73, v25
	v_exp_f32_e32 v57, v9
	v_exp_f32_e32 v74, v26
	v_exp_f32_e32 v58, v10
	v_exp_f32_e32 v75, v27
	v_exp_f32_e32 v59, v11
	v_exp_f32_e32 v76, v28
	v_exp_f32_e32 v60, v12
	v_exp_f32_e32 v77, v29
	v_exp_f32_e32 v61, v13
	v_exp_f32_e32 v78, v30
	v_exp_f32_e32 v62, v14
	v_exp_f32_e32 v79, v31
	v_exp_f32_e32 v63, v15
	v_exp_f32_e32 v80, v32
	v_exp_f32_e32 v64, v16
	v_exp_f32_e32 v81, v33
	v_exp_f32_e32 v65, v17
	s_lshl_b32 s4, s16, 2
	s_waitcnt vmcnt(4) lgkmcnt(0)
	s_barrier
	s_add_i32 s30, s4, 0
	v_cmp_gt_u32_e64 s[4:5], 32, v212
	s_mov_b64 s[14:15], 0
	s_mov_b64 s[16:17], 0x60000
	s_mov_b64 s[18:19], 0x78000
	v_mov_b32_e32 v2, v201
	v_mov_b32_e32 v3, v201
	v_mov_b32_e32 v4, v201
	v_mov_b32_e32 v5, v201
	v_mov_b32_e32 v6, v201
	v_mov_b32_e32 v7, v201
	v_mov_b32_e32 v8, v201
	v_mov_b32_e32 v9, v201
	v_mov_b32_e32 v10, v201
	v_mov_b32_e32 v11, v201
	v_mov_b32_e32 v12, v201
	v_mov_b32_e32 v13, v201
	v_mov_b32_e32 v14, v201
	v_mov_b32_e32 v15, v201
	v_mov_b32_e32 v16, v201
	v_mov_b32_e32 v17, v201
	v_mov_b32_e32 v18, v201
	v_mov_b32_e32 v19, v201
	v_mov_b32_e32 v20, v201
	v_mov_b32_e32 v21, v201
	v_mov_b32_e32 v22, v201
	v_mov_b32_e32 v23, v201
	v_mov_b32_e32 v24, v201
	v_mov_b32_e32 v25, v201
	v_mov_b32_e32 v26, v201
	v_mov_b32_e32 v27, v201
	v_mov_b32_e32 v28, v201
	v_mov_b32_e32 v29, v201
	v_mov_b32_e32 v30, v201
	v_mov_b32_e32 v31, v201
	v_mov_b32_e32 v32, v201
	v_mov_b32_e32 v33, v201
	v_lshl_add_u32 v217, v214, 2, s30
